# MLA: first key tile of each unit takes the exact-max path directly (no wasted carried-max attempt)
# baseline (speedup 1.0000x reference)
.LBB0_457:
	s_mov_b32 s101, 0
	s_lshl_b32 s5, s36, 8
	s_and_b32 s37, s5, 0xf00
	s_ashr_i32 s4, s36, 7
	s_xor_b32 s7, s37, 0x1f00
	v_readlane_b32 s5, v239, 14
	s_mov_b64 s[18:19], s[78:79]
	s_waitcnt vmcnt(0)
	v_mov_b32_e32 v66, v0
	s_add_i32 s41, s7, s5
	s_ashr_i32 s5, s4, 31
	s_lshl_b64 s[10:11], s[4:5], 13
	v_and_or_b32 v166, v66, 31, s41
	s_bfe_u32 s6, s36, 0x30004
	v_lshl_add_u64 v[174:175], s[10:11], 0, v[166:167]
	s_waitcnt vmcnt(0) lgkmcnt(0)
	v_mov_b64_e32 v[2:3], s[0:1]
	s_movk_i32 s12, 0xc00
	v_mad_u64_u32 v[2:3], s[8:9], v174, s12, v[2:3]
	s_mul_i32 s40, s6, 0xc0
	v_bfe_u32 v1, v66, 5, 1
	v_mad_i32_i24 v3, v175, s12, v3
	s_lshl_b32 s84, s40, 1
	v_lshl_add_u64 v[2:3], v[2:3], 0, s[84:85]
	v_lshlrev_b32_e32 v172, 4, v1
	v_mov_b32_e32 v173, v167
	v_lshl_add_u64 v[48:49], v[2:3], 0, v[172:173]
	v_lshlrev_b64 v[6:7], 8, v[174:175]
	global_load_dwordx4 v[16:19], v[48:49], off offset:256
	global_load_dwordx4 v[2:5], v[48:49], off offset:320
	v_lshl_add_u64 v[6:7], s[2:3], 0, v[6:7]
	v_lshlrev_b32_e32 v14, 5, v1
	v_mov_b32_e32 v15, v167
	v_lshl_add_u64 v[40:41], v[6:7], 0, v[14:15]
	global_load_dwordx4 v[20:23], v[40:41], off offset:128
	global_load_dwordx4 v[6:9], v[40:41], off offset:144
	global_load_dwordx4 v[24:27], v[40:41], off
	global_load_dwordx4 v[10:13], v[40:41], off offset:16
	v_lshlrev_b32_e32 v1, 2, v66
	v_lshrrev_b32_e32 v15, 1, v66
	v_and_b32_e32 v28, 3, v66
	v_and_b32_e32 v15, 12, v15
	v_and_b32_e32 v69, 16, v1
	v_or3_b32 v15, v15, v28, v69
	global_load_dwordx4 v[28:31], v[40:41], off offset:80
	global_load_dwordx4 v[32:35], v[40:41], off offset:64
	global_load_dwordx4 v[36:39], v[40:41], off offset:208
	s_nop 0
	global_load_dwordx4 v[40:43], v[40:41], off offset:192
	s_nop 0
	global_load_dwordx4 v[98:101], v[48:49], off
	global_load_dwordx4 v[102:105], v[48:49], off offset:32
	global_load_dwordx4 v[106:109], v[48:49], off offset:64
	global_load_dwordx4 v[110:113], v[48:49], off offset:96
	global_load_dwordx4 v[114:117], v[48:49], off offset:128
	global_load_dwordx4 v[118:121], v[48:49], off offset:160
	global_load_dwordx4 v[122:125], v[48:49], off offset:192
	global_load_dwordx4 v[126:129], v[48:49], off offset:224
	global_load_dwordx4 v[44:47], v[48:49], off offset:288
	s_nop 0
	global_load_dwordx4 v[48:51], v[48:49], off offset:352
	v_lshlrev_b32_e32 v67, 6, v66
	v_lshlrev_b32_e32 v68, 3, v66
	s_lshl_b32 s21, s6, 22
	s_lshl_b32 s20, s6, 8
	s_add_i32 s22, s7, 0x100
	v_and_b32_e32 v70, 0x78, v68
	s_mov_b32 s7, 0x7ffffc00
	s_lshl_b64 s[8:9], s[4:5], 24
	v_and_or_b32 v1, v67, s7, v70
	s_mov_b32 s23, 0x7fffc000
	v_lshlrev_b32_e32 v1, 1, v1
	s_barrier
	s_mov_b32 s47, 0
	v_mov_b32_e32 v207, 0xf149f2ca
	s_mov_b32 s101, 1
	v_mov_b32_e32 v205, 0
	s_mov_b32 s45, 63
	s_waitcnt vmcnt(19)
	v_lshlrev_b32_e32 v52, 16, v16
	v_and_b32_e32 v53, 0xffff0000, v16
	s_waitcnt vmcnt(18)
	v_lshlrev_b32_e32 v54, 16, v2
	v_and_b32_e32 v55, 0xffff0000, v2
	v_lshlrev_b32_e32 v16, 16, v17
	v_and_b32_e32 v17, 0xffff0000, v17
	v_lshlrev_b32_e32 v2, 16, v3
	v_and_b32_e32 v3, 0xffff0000, v3
	v_lshlrev_b32_e32 v56, 16, v18
	v_and_b32_e32 v57, 0xffff0000, v18
	v_lshlrev_b32_e32 v58, 16, v4
	v_and_b32_e32 v59, 0xffff0000, v4
	s_waitcnt vmcnt(17)
	v_pk_mul_f32 v[62:63], v[22:23], v[2:3]
	v_pk_mul_f32 v[22:23], v[22:23], v[16:17]
	s_waitcnt vmcnt(16)
	v_pk_mul_f32 v[64:65], v[6:7], v[58:59]
	v_pk_mul_f32 v[6:7], v[6:7], v[56:57]
	s_waitcnt vmcnt(15)
	v_pk_fma_f32 v[2:3], v[26:27], v[2:3], v[22:23]
	s_waitcnt vmcnt(14)
	v_pk_fma_f32 v[22:23], v[10:11], v[56:57], v[64:65] neg_lo:[0,0,1] neg_hi:[0,0,1]
	v_pk_fma_f32 v[6:7], v[10:11], v[58:59], v[6:7]
	v_add_u32_e32 v10, 0x8000, v67
	v_and_or_b32 v10, v10, s7, v70
	s_add_u32 s7, s28, s8
	v_lshlrev_b32_e32 v173, 1, v10
	v_lshlrev_b32_e32 v10, 11, v66
	v_and_b32_e32 v11, 56, v68
	s_addc_u32 s13, s29, s9
	s_lshl_b32 s42, s6, 7
	v_cvt_pk_bf16_f32 v132, v22, v23
	v_and_or_b32 v22, v10, s23, v11
	s_add_u32 s12, s7, s20
	v_lshlrev_b32_e32 v178, 1, v22
	s_addc_u32 s13, s13, 0
	v_mov_b32_e32 v22, v1
	global_load_dwordx4 v[134:137], v22, s[12:13]
	v_pk_fma_f32 v[16:17], v[26:27], v[16:17], v[62:63] neg_lo:[0,0,1] neg_hi:[0,0,1]
	s_lshl_b64 s[6:7], s[4:5], 20
	v_cvt_pk_bf16_f32 v131, v16, v17
	v_lshlrev_b32_e32 v17, 4, v66
	s_add_u32 s14, s30, s6
	v_ashrrev_i32_e32 v16, 3, v66
	v_and_b32_e32 v176, 0x70, v17
	s_addc_u32 s15, s31, s7
	v_mov_b32_e32 v22, v173
	v_lshl_or_b32 v177, v16, 7, v176
	s_add_u32 s16, s34, s21
	global_load_dwordx4 v[138:141], v22, s[12:13]
	s_addc_u32 s17, s35, 0
	s_lshl_b64 s[4:5], s[4:5], 14
	v_mov_b32_e32 v22, v177
	s_add_u32 s16, s16, s4
	v_add_u32_e32 v10, 0x100000, v10
	global_load_dwordx4 v[142:145], v22, s[14:15]
	s_addc_u32 s17, s17, s5
	v_mov_b32_e32 v22, v178
	v_and_or_b32 v10, v10, s23, v11
	global_load_dwordx4 v[154:157], v22, s[16:17]
	v_lshlrev_b32_e32 v179, 1, v10
	v_mov_b32_e32 v10, v179
	global_load_dwordx4 v[158:161], v10, s[16:17]
	v_lshlrev_b32_e32 v18, 16, v19
	v_and_b32_e32 v19, 0xffff0000, v19
	v_lshlrev_b32_e32 v4, 16, v5
	v_and_b32_e32 v5, 0xffff0000, v5
	v_pk_mul_f32 v[10:11], v[8:9], v[4:5]
	v_pk_mul_f32 v[8:9], v[8:9], v[18:19]
	v_cvt_pk_bf16_f32 v147, v2, v3
	v_pk_fma_f32 v[4:5], v[12:13], v[4:5], v[8:9]
	v_cvt_pk_bf16_f32 v148, v6, v7
	v_cvt_pk_bf16_f32 v149, v4, v5
	s_waitcnt vmcnt(5)
	v_lshlrev_b32_e32 v4, 16, v48
	v_and_b32_e32 v5, 0xffff0000, v48
	v_lshlrev_b32_e32 v2, 16, v44
	v_and_b32_e32 v3, 0xffff0000, v44
	v_pk_mul_f32 v[6:7], v[40:41], v[4:5]
	s_movk_i32 s23, 0x1a0
	v_pk_fma_f32 v[6:7], v[32:33], v[2:3], v[6:7] neg_lo:[0,0,1] neg_hi:[0,0,1]
	v_pk_mul_f32 v[2:3], v[40:41], v[2:3]
	v_and_b32_e32 v180, 0xf0, v17
	v_pk_fma_f32 v[2:3], v[32:33], v[4:5], v[2:3]
	v_cvt_pk_bf16_f32 v150, v6, v7
	v_cvt_pk_bf16_f32 v162, v2, v3
	v_ashrrev_i32_e32 v2, 4, v66
	v_mul_lo_u32 v181, v2, s23
	v_add_u32_e32 v3, 0, v181
	v_and_b32_e32 v182, 16, v2
	v_lshlrev_b32_e32 v6, 16, v49
	v_and_b32_e32 v7, 0xffff0000, v49
	v_add3_u32 v2, v3, v182, v180
	v_lshlrev_b32_e32 v4, 16, v45
	v_and_b32_e32 v5, 0xffff0000, v45
	v_pk_mul_f32 v[8:9], v[42:43], v[6:7]
	v_and_b32_e32 v185, 16, v16
	v_pk_fma_f32 v[8:9], v[34:35], v[4:5], v[8:9] neg_lo:[0,0,1] neg_hi:[0,0,1]
	v_pk_mul_f32 v[4:5], v[42:43], v[4:5]
	s_lshr_b32 s43, s22, 6
	v_pk_fma_f32 v[4:5], v[34:35], v[6:7], v[4:5]
	s_or_b32 s44, s41, 31
	v_cvt_pk_bf16_f32 v163, v4, v5
	v_pk_fma_f32 v[10:11], v[12:13], v[18:19], v[10:11] neg_lo:[0,0,1] neg_hi:[0,0,1]
	v_cvt_pk_bf16_f32 v151, v8, v9
	v_lshlrev_b32_e32 v8, 16, v50
	v_and_b32_e32 v9, 0xffff0000, v50
	s_add_u32 s4, s21, s4
	v_cvt_pk_bf16_f32 v133, v10, v11
	v_lshlrev_b32_e32 v6, 16, v46
	v_and_b32_e32 v7, 0xffff0000, v46
	v_pk_mul_f32 v[10:11], v[36:37], v[8:9]
	s_addc_u32 s5, 0, s5
	v_pk_fma_f32 v[10:11], v[28:29], v[6:7], v[10:11] neg_lo:[0,0,1] neg_hi:[0,0,1]
	s_waitcnt vmcnt(4)
	ds_write_b128 v2, v[134:137]
	v_add_u32_e32 v2, 0x200, v66
	v_ashrrev_i32_e32 v3, 4, v2
	v_mul_lo_u32 v183, v3, s23
	v_add_u32_e32 v4, 0, v183
	v_and_b32_e32 v184, 16, v3
	v_add3_u32 v3, v4, v184, v180
	v_lshlrev_b32_e32 v4, 8, v16
	v_ashrrev_i32_e32 v2, 3, v2
	v_and_b32_e32 v202, 16, v2
	s_add_u32 s4, s4, 0x10400080
	v_cvt_pk_bf16_f32 v152, v10, v11
	v_pk_mul_f32 v[6:7], v[36:37], v[6:7]
	s_waitcnt vmcnt(3)
	ds_write_b128 v3, v[138:141]
	v_mul_lo_u32 v3, v16, s23
	v_add3_u32 v3, 0, v3, v185
	v_add_u32_e32 v199, v3, v176
	s_movk_i32 s23, 0xa0
	v_sub_u32_e32 v3, v3, v4
	v_add_u32_e32 v3, v3, v176
	v_mul_lo_u32 v201, v2, s23
	s_waitcnt vmcnt(2)
	ds_write_b128 v199, v[142:145] offset:256
	v_lshlrev_b32_e32 v10, 16, v51
	v_and_b32_e32 v11, 0xffff0000, v51
	s_addc_u32 s5, s5, 0
	s_waitcnt vmcnt(1)
	ds_write_b128 v3, v[154:157] offset:53248
	v_add_u32_e32 v3, 0, v201
	v_add3_u32 v2, v3, v202, v176
	v_pk_fma_f32 v[6:7], v[28:29], v[8:9], v[6:7]
	v_lshlrev_b32_e32 v8, 16, v47
	v_and_b32_e32 v9, 0xffff0000, v47
	v_pk_mul_f32 v[12:13], v[38:39], v[10:11]
	s_waitcnt vmcnt(0)
	ds_write_b128 v2, v[158:161] offset:53248
	v_mul_u32_u24_e32 v2, 0x1a0, v15
	s_add_u32 s6, s6, 0xae02000
	v_pk_mul_f32 v[60:61], v[20:21], v[54:55]
	v_pk_mul_f32 v[20:21], v[20:21], v[52:53]
	v_pk_fma_f32 v[12:13], v[30:31], v[8:9], v[12:13] neg_lo:[0,0,1] neg_hi:[0,0,1]
	v_pk_mul_f32 v[8:9], v[38:39], v[8:9]
	v_add3_u32 v2, 0, v2, v69
	v_lshlrev_b32_e32 v3, 8, v15
	s_addc_u32 s7, s7, 0
	s_or_b32 s8, s8, s20
	v_pk_fma_f32 v[52:53], v[24:25], v[52:53], v[60:61] neg_lo:[0,0,1] neg_hi:[0,0,1]
	v_pk_fma_f32 v[20:21], v[24:25], v[54:55], v[20:21]
	v_pk_fma_f32 v[8:9], v[30:31], v[10:11], v[8:9]
	v_add_u32_e32 v203, v2, v172
	v_sub_u32_e32 v2, v2, v3
	s_add_u32 s8, s8, 0xe420000
	v_mov_b32_e32 v18, v167
	v_mov_b32_e32 v19, v167
	v_mov_b32_e32 v32, v167
	v_mov_b32_e32 v33, v167
	v_cvt_pk_bf16_f32 v130, v52, v53
	v_cvt_pk_bf16_f32 v146, v20, v21
	v_cvt_pk_bf16_f32 v153, v12, v13
	v_cvt_pk_bf16_f32 v164, v6, v7
	v_cvt_pk_bf16_f32 v165, v8, v9
	v_mul_lo_u32 v200, v16, s23
	v_add_u32_e32 v204, v2, v14
	s_addc_u32 s9, s9, 0
	v_mov_b32_e32 v20, v167
	v_mov_b32_e32 v21, v167
	v_mov_b32_e32 v22, v167
	v_mov_b32_e32 v23, v167
	v_mov_b32_e32 v24, v167
	v_mov_b32_e32 v25, v167
	v_mov_b32_e32 v26, v167
	v_mov_b32_e32 v27, v167
	v_mov_b32_e32 v28, v167
	v_mov_b32_e32 v29, v167
	v_mov_b32_e32 v30, v167
	v_mov_b32_e32 v31, v167
	v_mov_b64_e32 v[48:49], v[32:33]
	v_mov_b64_e32 v[64:65], v[32:33]
	v_mov_b64_e32 v[2:3], v[18:19]
	s_mov_b64 s[20:21], s[8:9]
	s_mov_b64 s[22:23], s[6:7]
	s_mov_b64 s[24:25], s[4:5]
	v_mov_b64_e32 v[46:47], v[30:31]
	v_mov_b64_e32 v[44:45], v[28:29]
	v_mov_b64_e32 v[42:43], v[26:27]
	v_mov_b64_e32 v[40:41], v[24:25]
	v_mov_b64_e32 v[38:39], v[22:23]
	v_mov_b64_e32 v[36:37], v[20:21]
	v_mov_b64_e32 v[34:35], v[18:19]
	v_mov_b64_e32 v[62:63], v[30:31]
	v_mov_b64_e32 v[60:61], v[28:29]
	v_mov_b64_e32 v[58:59], v[26:27]
	v_mov_b64_e32 v[56:57], v[24:25]
	v_mov_b64_e32 v[54:55], v[22:23]
	v_mov_b64_e32 v[52:53], v[20:21]
	v_mov_b64_e32 v[50:51], v[18:19]
	v_mov_b64_e32 v[4:5], v[20:21]
	v_mov_b64_e32 v[6:7], v[22:23]
	v_mov_b64_e32 v[8:9], v[24:25]
	v_mov_b64_e32 v[10:11], v[26:27]
	v_mov_b64_e32 v[12:13], v[28:29]
	v_mov_b64_e32 v[14:15], v[30:31]
	v_mov_b64_e32 v[16:17], v[32:33]
	s_waitcnt lgkmcnt(0)
	s_barrier
	v_and_b32_e32 v237, 64, v192
	v_xor_b32_e32 v236, 32, v192
	v_add_u32_e32 v237, 64, v237
	v_cmp_lt_i32_e32 vcc, v236, v237
	s_nop 1
	v_cndmask_b32_e32 v236, v192, v236, vcc
	v_lshlrev_b32_e32 v236, 2, v236

.LBB0_470:
	v_and_b32_e32 v66, 64, v192
	v_xor_b32_e32 v1, 32, v192
	v_add_u32_e32 v66, 64, v66
	v_cmp_lt_i32_e32 vcc, v1, v66
	s_lshl_b32 s84, s42, 1
	v_lshlrev_b32_e32 v166, 1, v172
	v_cndmask_b32_e32 v1, v192, v1, vcc
	v_lshlrev_b32_e32 v1, 2, v1
	ds_bpermute_b32 v66, v1, v205
	v_mov_b32_e32 v173, v167
	v_mov_b32_e32 v208, 0xf149f2ca
	s_mov_b32 s101, 1
	s_waitcnt lgkmcnt(0)
	v_add_f32_e32 v68, v205, v66
	v_div_scale_f32 v69, s[20:21], v68, v68, 1.0
	v_rcp_f32_e32 v70, v69
	v_div_scale_f32 v71, vcc, 1.0, v68, 1.0
	v_lshlrev_b64 v[66:67], 11, v[174:175]
	v_fma_f32 v72, -v69, v70, 1.0
	v_fmac_f32_e32 v70, v72, v70
	v_mul_f32_e32 v72, v71, v70
	v_fma_f32 v73, -v69, v72, v71
	v_fmac_f32_e32 v72, v73, v70
	v_fma_f32 v69, -v69, v72, v71
	v_div_fmas_f32 v69, v69, v70, v72
	v_lshl_add_u64 v[66:67], s[18:19], 0, v[66:67]
	v_div_fixup_f32 v68, v69, v68, 1.0
	v_lshl_add_u64 v[66:67], v[66:67], 0, s[84:85]
	v_lshl_add_u64 v[66:67], v[66:67], 0, v[166:167]
	s_mov_b64 s[18:19], 0x13200000
	v_pk_mul_f32 v[50:51], v[50:51], v[68:69] op_sel_hi:[1,0]
	v_pk_mul_f32 v[52:53], v[52:53], v[68:69] op_sel_hi:[1,0]
	v_lshl_add_u64 v[70:71], v[66:67], 0, s[18:19]
	v_cvt_pk_bf16_f32 v50, v50, v51
	v_cvt_pk_bf16_f32 v51, v52, v53
	v_pk_mul_f32 v[52:53], v[54:55], v[68:69] op_sel_hi:[1,0]
	v_pk_mul_f32 v[54:55], v[56:57], v[68:69] op_sel_hi:[1,0]
	s_mov_b32 s18, 0x13200000
	v_pk_mul_f32 v[34:35], v[34:35], v[68:69] op_sel_hi:[1,0]
	v_pk_mul_f32 v[36:37], v[36:37], v[68:69] op_sel_hi:[1,0]
	v_pk_mul_f32 v[18:19], v[18:19], v[68:69] op_sel_hi:[1,0]
	v_pk_mul_f32 v[20:21], v[20:21], v[68:69] op_sel_hi:[1,0]
	v_pk_mul_f32 v[2:3], v[2:3], v[68:69] op_sel_hi:[1,0]
	v_pk_mul_f32 v[4:5], v[4:5], v[68:69] op_sel_hi:[1,0]
	v_cvt_pk_bf16_f32 v52, v52, v53
	v_cvt_pk_bf16_f32 v53, v54, v55
	v_add_co_u32_e32 v54, vcc, s18, v66
	v_cvt_pk_bf16_f32 v34, v34, v35
	v_cvt_pk_bf16_f32 v35, v36, v37
	v_pk_mul_f32 v[36:37], v[38:39], v[68:69] op_sel_hi:[1,0]
	v_pk_mul_f32 v[38:39], v[40:41], v[68:69] op_sel_hi:[1,0]
	v_cvt_pk_bf16_f32 v18, v18, v19
	v_cvt_pk_bf16_f32 v19, v20, v21
	v_pk_mul_f32 v[20:21], v[22:23], v[68:69] op_sel_hi:[1,0]
	v_pk_mul_f32 v[22:23], v[24:25], v[68:69] op_sel_hi:[1,0]
	v_cvt_pk_bf16_f32 v2, v2, v3
	v_cvt_pk_bf16_f32 v3, v4, v5
	v_pk_mul_f32 v[4:5], v[6:7], v[68:69] op_sel_hi:[1,0]
	v_pk_mul_f32 v[6:7], v[8:9], v[68:69] op_sel_hi:[1,0]
	v_addc_co_u32_e32 v55, vcc, 0, v67, vcc
	v_cvt_pk_bf16_f32 v36, v36, v37
	v_cvt_pk_bf16_f32 v37, v38, v39
	v_cvt_pk_bf16_f32 v20, v20, v21
	v_cvt_pk_bf16_f32 v21, v22, v23
	v_cvt_pk_bf16_f32 v4, v4, v5
	v_cvt_pk_bf16_f32 v5, v6, v7
	global_store_dwordx4 v[54:55], v[50:53], off
	global_store_dwordx4 v[70:71], v[34:37], off offset:64
	global_store_dwordx4 v[70:71], v[18:21], off offset:128
	v_pk_mul_f32 v[50:51], v[58:59], v[68:69] op_sel_hi:[1,0]
	v_pk_mul_f32 v[52:53], v[60:61], v[68:69] op_sel_hi:[1,0]
	v_pk_mul_f32 v[34:35], v[42:43], v[68:69] op_sel_hi:[1,0]
	v_pk_mul_f32 v[36:37], v[44:45], v[68:69] op_sel_hi:[1,0]
	v_pk_mul_f32 v[18:19], v[26:27], v[68:69] op_sel_hi:[1,0]
	v_pk_mul_f32 v[20:21], v[28:29], v[68:69] op_sel_hi:[1,0]
	global_store_dwordx4 v[70:71], v[2:5], off offset:192
	v_cvt_pk_bf16_f32 v50, v50, v51
	v_cvt_pk_bf16_f32 v51, v52, v53
	v_pk_mul_f32 v[2:3], v[10:11], v[68:69] op_sel_hi:[1,0]
	v_pk_mul_f32 v[4:5], v[12:13], v[68:69] op_sel_hi:[1,0]
	v_pk_mul_f32 v[52:53], v[62:63], v[68:69] op_sel_hi:[1,0]
	v_pk_mul_f32 v[54:55], v[64:65], v[68:69] op_sel_hi:[1,0]
	v_cvt_pk_bf16_f32 v34, v34, v35
	v_cvt_pk_bf16_f32 v35, v36, v37
	v_pk_mul_f32 v[36:37], v[46:47], v[68:69] op_sel_hi:[1,0]
	v_pk_mul_f32 v[38:39], v[48:49], v[68:69] op_sel_hi:[1,0]
	v_cvt_pk_bf16_f32 v18, v18, v19
	v_cvt_pk_bf16_f32 v19, v20, v21
	v_pk_mul_f32 v[20:21], v[30:31], v[68:69] op_sel_hi:[1,0]
	v_pk_mul_f32 v[22:23], v[32:33], v[68:69] op_sel_hi:[1,0]
	v_cvt_pk_bf16_f32 v2, v2, v3
	v_cvt_pk_bf16_f32 v3, v4, v5
	v_pk_mul_f32 v[4:5], v[14:15], v[68:69] op_sel_hi:[1,0]
	v_pk_mul_f32 v[6:7], v[16:17], v[68:69] op_sel_hi:[1,0]
	v_readlane_b32 s20, v239, 14
	v_cvt_pk_bf16_f32 v52, v52, v53
	v_cvt_pk_bf16_f32 v53, v54, v55
	v_cvt_pk_bf16_f32 v36, v36, v37
	v_cvt_pk_bf16_f32 v37, v38, v39
	v_cvt_pk_bf16_f32 v20, v20, v21
	v_cvt_pk_bf16_f32 v21, v22, v23
	v_cvt_pk_bf16_f32 v4, v4, v5
	v_cvt_pk_bf16_f32 v5, v6, v7
	s_mov_b64 s[18:19], s[78:79]
	v_mov_b32_e32 v58, v0
	s_add_i32 s20, s37, s20
	global_store_dwordx4 v[70:71], v[50:53], off offset:16
	global_store_dwordx4 v[70:71], v[34:37], off offset:80
	global_store_dwordx4 v[70:71], v[18:21], off offset:144
	global_store_dwordx4 v[70:71], v[2:5], off offset:208
	s_movk_i32 s21, 0xc00
	v_and_or_b32 v166, v58, 31, s20
	v_lshl_add_u64 v[174:175], s[10:11], 0, v[166:167]
	v_mov_b64_e32 v[2:3], s[0:1]
	v_mad_u64_u32 v[2:3], s[10:11], v174, s21, v[2:3]
	v_bfe_u32 v14, v58, 5, 1
	v_mad_i32_i24 v3, v175, s21, v3
	s_lshl_b32 s10, s40, 1
	s_mov_b32 s11, s85
	v_lshl_add_u64 v[2:3], v[2:3], 0, s[10:11]
	v_lshlrev_b32_e32 v172, 4, v14
	v_lshl_add_u64 v[32:33], v[2:3], 0, v[172:173]
	global_load_dwordx4 v[4:7], v[32:33], off offset:256
	global_load_dwordx4 v[8:11], v[32:33], off offset:320
	v_lshlrev_b64 v[2:3], 8, v[174:175]
	v_lshl_add_u64 v[12:13], s[2:3], 0, v[2:3]
	v_lshlrev_b32_e32 v2, 5, v14
	v_mov_b32_e32 v3, v167
	v_lshl_add_u64 v[48:49], v[12:13], 0, v[2:3]
	global_load_dwordx4 v[12:15], v[48:49], off offset:128
	global_load_dwordx4 v[16:19], v[48:49], off
	global_load_dwordx4 v[20:23], v[48:49], off offset:144
	global_load_dwordx4 v[24:27], v[48:49], off offset:16
	v_lshlrev_b32_e32 v3, 2, v58
	v_lshrrev_b32_e32 v28, 1, v58
	v_and_b32_e32 v28, 12, v28
	v_and_b32_e32 v29, 3, v58
	v_and_b32_e32 v3, 16, v3
	global_load_dwordx4 v[98:101], v[32:33], off
	global_load_dwordx4 v[102:105], v[32:33], off offset:32
	global_load_dwordx4 v[106:109], v[32:33], off offset:64
	global_load_dwordx4 v[110:113], v[32:33], off offset:96
	global_load_dwordx4 v[114:117], v[32:33], off offset:128
	global_load_dwordx4 v[118:121], v[32:33], off offset:160
	global_load_dwordx4 v[122:125], v[32:33], off offset:192
	global_load_dwordx4 v[126:129], v[32:33], off offset:224
	v_or3_b32 v59, v28, v29, v3
	global_load_dwordx4 v[28:31], v[32:33], off offset:288
	s_nop 0
	global_load_dwordx4 v[32:35], v[32:33], off offset:352
	s_nop 0
	global_load_dwordx4 v[36:39], v[48:49], off offset:80
	global_load_dwordx4 v[40:43], v[48:49], off offset:64
	global_load_dwordx4 v[44:47], v[48:49], off offset:208
	s_nop 0
	global_load_dwordx4 v[48:51], v[48:49], off offset:192
	s_mov_b32 s10, 0x7ffffc00
	s_barrier
	s_addk_i32 s37, 0x100
	s_mov_b32 s21, 1
	v_mov_b32_e32 v205, 0
	s_waitcnt vmcnt(19)
	v_lshlrev_b32_e32 v52, 16, v4
	v_and_b32_e32 v53, 0xffff0000, v4
	s_waitcnt vmcnt(18)
	v_lshlrev_b32_e32 v54, 16, v8
	v_and_b32_e32 v55, 0xffff0000, v8
	s_waitcnt vmcnt(17)
	v_pk_mul_f32 v[56:57], v[12:13], v[54:55]
	v_pk_mul_f32 v[12:13], v[12:13], v[52:53]
	v_lshlrev_b32_e32 v8, 16, v9
	v_and_b32_e32 v9, 0xffff0000, v9
	s_waitcnt vmcnt(16)
	v_pk_fma_f32 v[56:57], v[16:17], v[52:53], v[56:57] neg_lo:[0,0,1] neg_hi:[0,0,1]
	v_pk_fma_f32 v[12:13], v[16:17], v[54:55], v[12:13]
	v_lshlrev_b32_e32 v4, 16, v5
	v_and_b32_e32 v5, 0xffff0000, v5
	v_pk_mul_f32 v[16:17], v[14:15], v[8:9]
	v_cvt_pk_bf16_f32 v146, v12, v13
	v_pk_fma_f32 v[16:17], v[18:19], v[4:5], v[16:17] neg_lo:[0,0,1] neg_hi:[0,0,1]
	v_pk_mul_f32 v[4:5], v[14:15], v[4:5]
	v_lshlrev_b32_e32 v14, 16, v10
	v_and_b32_e32 v15, 0xffff0000, v10
	v_cvt_pk_bf16_f32 v131, v16, v17
	v_pk_fma_f32 v[4:5], v[18:19], v[8:9], v[4:5]
	v_lshlrev_b32_e32 v8, 16, v6
	v_and_b32_e32 v9, 0xffff0000, v6
	s_waitcnt vmcnt(15)
	v_pk_mul_f32 v[16:17], v[20:21], v[14:15]
	v_lshlrev_b32_e32 v10, 16, v11
	s_waitcnt vmcnt(14)
	v_pk_fma_f32 v[16:17], v[24:25], v[8:9], v[16:17] neg_lo:[0,0,1] neg_hi:[0,0,1]
	v_pk_mul_f32 v[8:9], v[20:21], v[8:9]
	v_cvt_pk_bf16_f32 v132, v16, v17
	v_pk_fma_f32 v[8:9], v[24:25], v[14:15], v[8:9]
	v_lshlrev_b32_e32 v15, 3, v58
	v_lshlrev_b32_e32 v14, 6, v58
	v_and_b32_e32 v16, 0x78, v15
	v_and_or_b32 v17, v14, s10, v16
	v_add_u32_e32 v14, 0x8000, v14
	v_lshlrev_b32_e32 v173, 1, v17
	v_and_or_b32 v14, v14, s10, v16
	v_lshlrev_b32_e32 v176, 1, v14
	v_mov_b32_e32 v14, v173
	global_load_dwordx4 v[134:137], v14, s[12:13]
	v_lshlrev_b32_e32 v17, 4, v58
	v_ashrrev_i32_e32 v16, 3, v58
	v_and_b32_e32 v177, 0x70, v17
	v_lshl_or_b32 v178, v16, 7, v177
	v_mov_b32_e32 v14, v176
	v_mov_b32_e32 v18, v178
	global_load_dwordx4 v[138:141], v14, s[12:13]
	v_lshlrev_b32_e32 v14, 11, v58
	v_and_b32_e32 v15, 56, v15
	s_mov_b32 s10, 0x7fffc000
	global_load_dwordx4 v[142:145], v18, s[14:15]
	v_and_or_b32 v18, v14, s10, v15
	v_lshlrev_b32_e32 v179, 1, v18
	v_add_u32_e32 v14, 0x100000, v14
	v_mov_b32_e32 v18, v179
	v_and_or_b32 v14, v14, s10, v15
	global_load_dwordx4 v[154:157], v18, s[16:17]
	v_lshlrev_b32_e32 v180, 1, v14
	v_mov_b32_e32 v14, v180
	global_load_dwordx4 v[158:161], v14, s[16:17]
	v_and_b32_e32 v11, 0xffff0000, v11
	v_lshlrev_b32_e32 v6, 16, v7
	v_and_b32_e32 v7, 0xffff0000, v7
	v_pk_mul_f32 v[14:15], v[22:23], v[10:11]
	v_cvt_pk_bf16_f32 v147, v4, v5
	v_pk_fma_f32 v[14:15], v[26:27], v[6:7], v[14:15] neg_lo:[0,0,1] neg_hi:[0,0,1]
	v_pk_mul_f32 v[6:7], v[22:23], v[6:7]
	v_cvt_pk_bf16_f32 v148, v8, v9
	v_pk_fma_f32 v[6:7], v[26:27], v[10:11], v[6:7]
	s_waitcnt vmcnt(10)
	v_lshlrev_b32_e32 v4, 16, v28
	v_cvt_pk_bf16_f32 v149, v6, v7
	s_waitcnt vmcnt(9)
	v_lshlrev_b32_e32 v6, 16, v32
	v_and_b32_e32 v7, 0xffff0000, v32
	v_and_b32_e32 v5, 0xffff0000, v28
	s_waitcnt vmcnt(5)
	v_pk_mul_f32 v[8:9], v[48:49], v[6:7]
	s_movk_i32 s10, 0x1a0
	v_pk_fma_f32 v[8:9], v[40:41], v[4:5], v[8:9] neg_lo:[0,0,1] neg_hi:[0,0,1]
	v_pk_mul_f32 v[4:5], v[48:49], v[4:5]
	v_and_b32_e32 v181, 0xf0, v17
	v_pk_fma_f32 v[4:5], v[40:41], v[6:7], v[4:5]
	v_cvt_pk_bf16_f32 v150, v8, v9
	v_cvt_pk_bf16_f32 v162, v4, v5
	v_ashrrev_i32_e32 v4, 4, v58
	v_mul_lo_u32 v182, v4, s10
	v_add_u32_e32 v5, 0, v182
	v_and_b32_e32 v183, 16, v4
	v_lshlrev_b32_e32 v8, 16, v33
	v_and_b32_e32 v9, 0xffff0000, v33
	v_add3_u32 v4, v5, v183, v181
	v_lshlrev_b32_e32 v6, 16, v29
	v_and_b32_e32 v7, 0xffff0000, v29
	v_pk_mul_f32 v[10:11], v[50:51], v[8:9]
	v_and_b32_e32 v199, 16, v16
	v_pk_fma_f32 v[10:11], v[42:43], v[6:7], v[10:11] neg_lo:[0,0,1] neg_hi:[0,0,1]
	v_pk_mul_f32 v[6:7], v[50:51], v[6:7]
	v_cvt_pk_bf16_f32 v151, v10, v11
	v_pk_fma_f32 v[6:7], v[42:43], v[8:9], v[6:7]
	v_lshlrev_b32_e32 v10, 16, v34
	v_cvt_pk_bf16_f32 v163, v6, v7
	v_and_b32_e32 v11, 0xffff0000, v34
	v_lshlrev_b32_e32 v8, 16, v30
	v_and_b32_e32 v9, 0xffff0000, v30
	v_pk_mul_f32 v[12:13], v[44:45], v[10:11]
	v_cvt_pk_bf16_f32 v133, v14, v15
	v_pk_fma_f32 v[12:13], v[36:37], v[8:9], v[12:13] neg_lo:[0,0,1] neg_hi:[0,0,1]
	v_pk_mul_f32 v[8:9], v[44:45], v[8:9]
	v_cvt_pk_bf16_f32 v152, v12, v13
	v_lshlrev_b32_e32 v12, 16, v35
	v_and_b32_e32 v13, 0xffff0000, v35
	v_pk_fma_f32 v[8:9], v[36:37], v[10:11], v[8:9]
	v_lshlrev_b32_e32 v10, 16, v31
	v_and_b32_e32 v11, 0xffff0000, v31
	v_pk_mul_f32 v[14:15], v[46:47], v[12:13]
	v_mov_b32_e32 v18, v167
	v_pk_fma_f32 v[14:15], v[38:39], v[10:11], v[14:15] neg_lo:[0,0,1] neg_hi:[0,0,1]
	s_waitcnt vmcnt(4)
	ds_write_b128 v4, v[134:137]
	v_add_u32_e32 v4, 0x200, v58
	v_ashrrev_i32_e32 v5, 4, v4
	v_mul_lo_u32 v184, v5, s10
	v_add_u32_e32 v6, 0, v184
	v_and_b32_e32 v185, 16, v5
	v_add3_u32 v5, v6, v185, v181
	v_lshlrev_b32_e32 v6, 8, v16
	s_waitcnt vmcnt(3)
	ds_write_b128 v5, v[138:141]
	v_mul_lo_u32 v5, v16, s10
	v_add3_u32 v5, 0, v5, v199
	v_add_u32_e32 v200, v5, v177
	s_movk_i32 s10, 0xa0
	v_sub_u32_e32 v5, v5, v6
	v_ashrrev_i32_e32 v4, 3, v4
	v_add_u32_e32 v5, v5, v177
	v_mul_lo_u32 v202, v4, s10
	s_waitcnt vmcnt(2)
	ds_write_b128 v200, v[142:145] offset:256
	v_and_b32_e32 v203, 16, v4
	v_pk_mul_f32 v[10:11], v[46:47], v[10:11]
	s_waitcnt vmcnt(1)
	ds_write_b128 v5, v[154:157] offset:53248
	v_add_u32_e32 v5, 0, v202
	v_add3_u32 v4, v5, v203, v177
	v_pk_fma_f32 v[10:11], v[38:39], v[12:13], v[10:11]
	s_waitcnt vmcnt(0)
	ds_write_b128 v4, v[158:161] offset:53248
	v_mul_u32_u24_e32 v4, 0x1a0, v59
	v_add3_u32 v3, 0, v4, v3
	v_lshlrev_b32_e32 v4, 8, v59
	v_add_u32_e32 v204, v3, v172
	v_sub_u32_e32 v3, v3, v4
	v_mov_b32_e32 v19, v167
	v_mov_b32_e32 v32, v167
	v_mov_b32_e32 v33, v167
	v_cvt_pk_bf16_f32 v130, v56, v57
	v_cvt_pk_bf16_f32 v153, v14, v15
	v_cvt_pk_bf16_f32 v164, v8, v9
	v_cvt_pk_bf16_f32 v165, v10, v11
	v_mul_lo_u32 v201, v16, s10
	v_add_u32_e32 v206, v3, v2
	v_mov_b32_e32 v20, v167
	v_mov_b32_e32 v21, v167
	v_mov_b32_e32 v22, v167
	v_mov_b32_e32 v23, v167
	v_mov_b32_e32 v24, v167
	v_mov_b32_e32 v25, v167
	v_mov_b32_e32 v26, v167
	v_mov_b32_e32 v27, v167
	v_mov_b32_e32 v28, v167
	v_mov_b32_e32 v29, v167
	v_mov_b32_e32 v30, v167
	v_mov_b32_e32 v31, v167
	v_mov_b64_e32 v[48:49], v[32:33]
	v_mov_b64_e32 v[64:65], v[32:33]
	v_mov_b64_e32 v[2:3], v[18:19]
	s_lshr_b32 s14, s37, 6
	s_or_b32 s15, s20, 31
	s_mov_b32 s16, 63
	v_mov_b64_e32 v[46:47], v[30:31]
	v_mov_b64_e32 v[44:45], v[28:29]
	v_mov_b64_e32 v[42:43], v[26:27]
	v_mov_b64_e32 v[40:41], v[24:25]
	v_mov_b64_e32 v[38:39], v[22:23]
	v_mov_b64_e32 v[36:37], v[20:21]
	v_mov_b64_e32 v[34:35], v[18:19]
	v_mov_b64_e32 v[62:63], v[30:31]
	v_mov_b64_e32 v[60:61], v[28:29]
	v_mov_b64_e32 v[58:59], v[26:27]
	v_mov_b64_e32 v[56:57], v[24:25]
	v_mov_b64_e32 v[54:55], v[22:23]
	v_mov_b64_e32 v[52:53], v[20:21]
	v_mov_b64_e32 v[50:51], v[18:19]
	v_mov_b64_e32 v[4:5], v[20:21]
	v_mov_b64_e32 v[6:7], v[22:23]
	v_mov_b64_e32 v[8:9], v[24:25]
	v_mov_b64_e32 v[10:11], v[26:27]
	v_mov_b64_e32 v[12:13], v[28:29]
	v_mov_b64_e32 v[14:15], v[30:31]
	v_mov_b64_e32 v[16:17], v[32:33]
	s_waitcnt lgkmcnt(0)
	s_barrier
